# speedup vs baseline: 1.0142x; 1.0014x over previous
.LBB6_28:
	s_or_b64 exec, exec, s[2:3]
	v_lshlrev_b32_e32 v39, 4, v0
	v_and_b32_e32 v19, 32, v0
	s_load_dwordx4 s[4:7], s[0:1], 0x1c
	v_bitop3_b32 v19, v39, v19, 48 bitop3:0x6c
	v_and_or_b32 v19, v0, 64, v19
	v_lshrrev_b32_e32 v20, 1, v19
	v_lshrrev_b32_e32 v19, 1, v0
	v_lshrrev_b32_e32 v22, 5, v0
	v_bfe_u32 v21, v0, 2, 4
	v_and_b32_e32 v19, 24, v19
	v_and_b32_e32 v22, 4, v22
	v_bfe_u32 v23, v0, 2, 2
	v_lshrrev_b32_e32 v24, 3, v0
	v_or3_b32 v19, v23, v22, v19
	v_and_or_b32 v22, v24, 48, v21
	s_waitcnt lgkmcnt(0)
	v_mad_u64_u32 v[22:23], s[2:3], v22, s4, v[20:21]
	v_and_or_b32 v23, v24, 32, v19
	v_mad_u64_u32 v[24:25], s[2:3], v23, s5, v[20:21]
	v_bfe_u32 v23, v0, 3, 25
	v_or_b32_e32 v23, 64, v23
	s_movk_i32 s2, 0x70
	v_and_or_b32 v21, v23, s2, v21
	v_mad_u64_u32 v[28:29], s[2:3], v21, s4, v[20:21]
	s_movk_i32 s2, 0x60
	s_nop 0
	v_and_or_b32 v19, v23, s2, v19
	v_mad_u64_u32 v[20:21], s[2:3], v19, s5, v[20:21]
	s_mul_hi_i32 s3, s5, s13
	s_mul_i32 s2, s5, s13
	s_lshl_b64 s[2:3], s[2:3], 1
	s_add_u32 s2, s10, s2
	s_addc_u32 s3, s11, s3
	s_add_i32 s7, 0, 0x10000
	v_add_u32_e32 v36, s7, v39
	v_mov_b32_e32 v25, v18
	v_mov_b32_e32 v21, v18
	v_lshlrev_b64 v[24:25], 1, v[24:25]
	v_readfirstlane_b32 s7, v36
	v_lshlrev_b64 v[20:21], 1, v[20:21]
	v_add_u32_e32 v19, 0x2000, v36
	v_lshl_add_u64 v[30:31], s[2:3], 0, v[24:25]
	s_mov_b32 m0, s7
	v_lshl_add_u64 v[32:33], s[2:3], 0, v[20:21]
	v_readfirstlane_b32 s2, v19
	global_load_lds_dwordx4 v[30:31], off
	s_mov_b32 m0, s2
	s_mul_hi_i32 s3, s4, s12
	s_mul_i32 s2, s4, s12
	s_lshl_b64 s[2:3], s[2:3], 1
	s_add_u32 s2, s8, s2
	v_add_u32_e32 v35, 0, v39
	v_mov_b32_e32 v23, v18
	v_mov_b32_e32 v29, v18
	s_addc_u32 s3, s9, s3
	v_lshlrev_b64 v[40:41], 1, v[22:23]
	v_readfirstlane_b32 s7, v35
	v_lshlrev_b64 v[42:43], 1, v[28:29]
	v_add_u32_e32 v18, 0x2000, v35
	global_load_lds_dwordx4 v[32:33], off
	v_lshl_add_u64 v[26:27], s[2:3], 0, v[40:41]
	s_mov_b32 m0, s7
	v_lshl_add_u64 v[28:29], s[2:3], 0, v[42:43]
	v_readfirstlane_b32 s2, v18
	global_load_lds_dwordx4 v[26:27], off
	s_mov_b32 m0, s2
	s_or_b32 s2, s13, 0x80
	s_mul_hi_i32 s3, s5, s2
	s_mul_i32 s2, s5, s2
	s_lshl_b64 s[2:3], s[2:3], 1
	s_add_u32 s2, s10, s2
	s_addc_u32 s3, s11, s3
	s_add_i32 s5, 0, 0x14000
	v_add_u32_e32 v34, s5, v39
	v_add_u32_e32 v18, 0x2000, v34
	v_readfirstlane_b32 s5, v34
	global_load_lds_dwordx4 v[28:29], off
	v_lshl_add_u64 v[22:23], s[2:3], 0, v[24:25]
	s_mov_b32 m0, s5
	v_lshl_add_u64 v[24:25], s[2:3], 0, v[20:21]
	v_readfirstlane_b32 s2, v18
	global_load_lds_dwordx4 v[22:23], off
	s_mov_b32 m0, s2
	s_or_b32 s2, s12, 0x80
	s_mul_hi_i32 s3, s4, s2
	s_mul_i32 s2, s4, s2
	s_lshl_b64 s[2:3], s[2:3], 1
	s_add_u32 s2, s8, s2
	s_addc_u32 s3, s9, s3
	v_add_u32_e32 v20, 0x4000, v35
	v_lshl_add_u64 v[18:19], s[2:3], 0, v[40:41]
	v_readfirstlane_b32 s4, v20
	v_add_u32_e32 v40, 0x6000, v35
	global_load_lds_dwordx4 v[24:25], off
	s_mov_b32 m0, s4
	v_lshl_add_u64 v[20:21], s[2:3], 0, v[42:43]
	v_readfirstlane_b32 s2, v40
	global_load_lds_dwordx4 v[18:19], off
	s_mov_b32 m0, s2
	s_nop 0
	global_load_lds_dwordx4 v[20:21], off
	s_and_saveexec_b64 s[4:5], vcc
	s_cbranch_execz .LBB6_30
	s_waitcnt vmcnt(8)
	v_pk_add_f32 v[14:15], v[14:15], v[16:17]
	s_mov_b32 s2, 0x3b000000
	v_pk_add_f32 v[10:11], v[10:11], v[14:15]
	s_nop 0
	v_pk_add_f32 v[10:11], v[12:13], v[10:11]
	s_nop 0
	v_pk_add_f32 v[6:7], v[6:7], v[10:11]
	s_nop 0
	v_pk_add_f32 v[6:7], v[8:9], v[6:7]
	s_nop 0
	v_pk_add_f32 v[2:3], v[2:3], v[6:7]
	s_nop 0
	v_pk_add_f32 v[2:3], v[4:5], v[2:3]
	s_nop 0
	v_pk_mul_f32 v[2:3], v[2:3], s[2:3] op_sel_hi:[1,0]
	s_mov_b32 s2, 0x800000
	v_fma_f32 v3, -v2, v2, v3
	v_max_f32_e32 v3, 0, v3
	v_add_f32_e32 v3, 0x3727c5ac, v3
	v_mul_f32_e32 v4, 0x4b800000, v3
	v_cmp_gt_f32_e64 s[2:3], s2, v3
	s_nop 1
	v_cndmask_b32_e64 v3, v3, v4, s[2:3]
	v_rsq_f32_e32 v3, v3
	s_nop 0
	v_mul_f32_e32 v4, 0x45800000, v3
	v_cndmask_b32_e64 v3, v3, v4, s[2:3]
	v_lshl_add_u32 v4, v0, 3, 0
	v_add_u32_e32 v4, 0x20000, v4
	ds_write_b64 v4, v[2:3]
	v_lshl_add_u32 v2, v0, 2, 0
	v_add_u32_e32 v3, 0x20800, v2
	v_add_u32_e32 v2, 0x20c00, v2
	ds_write_b32 v3, v38
	ds_write_b32 v2, v37

.LBB8_2:
	s_or_b64 exec, exec, s[2:3]
	v_lshlrev_b32_e32 v38, 4, v0
	v_and_b32_e32 v19, 32, v0
	s_load_dwordx4 s[4:7], s[0:1], 0x1c
	v_bitop3_b32 v19, v38, v19, 48 bitop3:0x6c
	v_and_or_b32 v19, v0, 64, v19
	v_lshrrev_b32_e32 v20, 1, v19
	v_lshrrev_b32_e32 v19, 1, v0
	v_lshrrev_b32_e32 v22, 5, v0
	v_bfe_u32 v21, v0, 2, 4
	v_and_b32_e32 v19, 24, v19
	v_and_b32_e32 v22, 4, v22
	v_bfe_u32 v23, v0, 2, 2
	v_lshrrev_b32_e32 v24, 3, v0
	v_or3_b32 v19, v23, v22, v19
	v_and_or_b32 v22, v24, 48, v21
	s_waitcnt lgkmcnt(0)
	v_mad_u64_u32 v[22:23], s[2:3], v22, s4, v[20:21]
	v_and_or_b32 v23, v24, 32, v19
	v_mad_u64_u32 v[24:25], s[2:3], v23, s5, v[20:21]
	v_bfe_u32 v23, v0, 3, 25
	v_or_b32_e32 v23, 64, v23
	s_movk_i32 s2, 0x70
	v_and_or_b32 v21, v23, s2, v21
	v_mad_u64_u32 v[28:29], s[2:3], v21, s4, v[20:21]
	s_movk_i32 s2, 0x60
	s_nop 0
	v_and_or_b32 v19, v23, s2, v19
	v_mad_u64_u32 v[20:21], s[2:3], v19, s5, v[20:21]
	s_mul_hi_i32 s3, s5, s13
	s_mul_i32 s2, s5, s13
	s_lshl_b64 s[2:3], s[2:3], 1
	s_add_u32 s2, s10, s2
	s_addc_u32 s3, s11, s3
	s_add_i32 s7, 0, 0x10000
	v_add_u32_e32 v36, s7, v38
	v_mov_b32_e32 v25, v18
	v_mov_b32_e32 v21, v18
	v_lshlrev_b64 v[24:25], 1, v[24:25]
	v_readfirstlane_b32 s7, v36
	v_lshlrev_b64 v[20:21], 1, v[20:21]
	v_add_u32_e32 v19, 0x2000, v36
	v_lshl_add_u64 v[30:31], s[2:3], 0, v[24:25]
	s_mov_b32 m0, s7
	v_lshl_add_u64 v[32:33], s[2:3], 0, v[20:21]
	v_readfirstlane_b32 s2, v19
	global_load_lds_dwordx4 v[30:31], off
	s_mov_b32 m0, s2
	s_mul_hi_i32 s3, s4, s12
	s_mul_i32 s2, s4, s12
	s_lshl_b64 s[2:3], s[2:3], 1
	s_add_u32 s2, s8, s2
	v_add_u32_e32 v35, 0, v38
	v_mov_b32_e32 v23, v18
	v_mov_b32_e32 v29, v18
	s_addc_u32 s3, s9, s3
	v_lshlrev_b64 v[40:41], 1, v[22:23]
	v_readfirstlane_b32 s7, v35
	v_lshlrev_b64 v[42:43], 1, v[28:29]
	v_add_u32_e32 v18, 0x2000, v35
	global_load_lds_dwordx4 v[32:33], off
	v_lshl_add_u64 v[26:27], s[2:3], 0, v[40:41]
	s_mov_b32 m0, s7
	v_lshl_add_u64 v[28:29], s[2:3], 0, v[42:43]
	v_readfirstlane_b32 s2, v18
	global_load_lds_dwordx4 v[26:27], off
	s_mov_b32 m0, s2
	s_or_b32 s2, s13, 0x80
	s_mul_hi_i32 s3, s5, s2
	s_mul_i32 s2, s5, s2
	s_lshl_b64 s[2:3], s[2:3], 1
	s_add_u32 s2, s10, s2
	s_addc_u32 s3, s11, s3
	s_add_i32 s5, 0, 0x14000
	v_add_u32_e32 v34, s5, v38
	v_add_u32_e32 v18, 0x2000, v34
	v_readfirstlane_b32 s5, v34
	global_load_lds_dwordx4 v[28:29], off
	v_lshl_add_u64 v[22:23], s[2:3], 0, v[24:25]
	s_mov_b32 m0, s5
	v_lshl_add_u64 v[24:25], s[2:3], 0, v[20:21]
	v_readfirstlane_b32 s2, v18
	global_load_lds_dwordx4 v[22:23], off
	s_mov_b32 m0, s2
	s_or_b32 s2, s12, 0x80
	s_mul_hi_i32 s3, s4, s2
	s_mul_i32 s2, s4, s2
	s_lshl_b64 s[2:3], s[2:3], 1
	s_add_u32 s2, s8, s2
	v_add_u32_e32 v20, 0x4000, v35
	s_addc_u32 s3, s9, s3
	v_readfirstlane_b32 s4, v20
	v_add_u32_e32 v39, 0x6000, v35
	global_load_lds_dwordx4 v[24:25], off
	v_lshl_add_u64 v[18:19], s[2:3], 0, v[40:41]
	s_mov_b32 m0, s4
	v_lshl_add_u64 v[20:21], s[2:3], 0, v[42:43]
	v_readfirstlane_b32 s2, v39
	global_load_lds_dwordx4 v[18:19], off
	s_mov_b32 m0, s2
	s_nop 0
	global_load_lds_dwordx4 v[20:21], off
	s_and_saveexec_b64 s[4:5], vcc
	s_cbranch_execz .LBB8_4
	s_waitcnt vmcnt(8)
	v_pk_add_f32 v[14:15], v[14:15], v[16:17]
	s_mov_b32 s2, 0x3b000000
	v_pk_add_f32 v[10:11], v[10:11], v[14:15]
	s_nop 0
	v_pk_add_f32 v[10:11], v[12:13], v[10:11]
	s_nop 0
	v_pk_add_f32 v[6:7], v[6:7], v[10:11]
	s_nop 0
	v_pk_add_f32 v[6:7], v[8:9], v[6:7]
	s_nop 0
	v_pk_add_f32 v[2:3], v[2:3], v[6:7]
	s_nop 0
	v_pk_add_f32 v[2:3], v[4:5], v[2:3]
	s_nop 0
	v_pk_mul_f32 v[2:3], v[2:3], s[2:3] op_sel_hi:[1,0]
	s_mov_b32 s2, 0x800000
	v_fma_f32 v3, -v2, v2, v3
	v_max_f32_e32 v3, 0, v3
	v_add_f32_e32 v3, 0x3727c5ac, v3
	v_mul_f32_e32 v4, 0x4b800000, v3
	v_cmp_gt_f32_e64 s[2:3], s2, v3
	s_nop 1
	v_cndmask_b32_e64 v3, v3, v4, s[2:3]
	v_rsq_f32_e32 v3, v3
	s_nop 0
	v_mul_f32_e32 v4, 0x45800000, v3
	v_cndmask_b32_e64 v3, v3, v4, s[2:3]
	v_lshl_add_u32 v4, v0, 3, 0
	v_add_u32_e32 v4, 0x20000, v4
	ds_write_b64 v4, v[2:3]
	v_lshl_add_u32 v2, v0, 2, 0
	v_add_u32_e32 v3, 0x20800, v2
	v_add_u32_e32 v2, 0x20c00, v2
	ds_write_b32 v3, v37
	ds_write_b32 v2, v1
